# gdn_local: gate-input math deferred behind the row loads (one memory latency per unit instead of two on waves 0-1)
# baseline (speedup 1.0000x reference)
.LBB0_304:
	s_lshl_b32 s0, s18, 2
	s_sub_i32 s16, s2, s0
	v_mov_b32_e32 v121, v167
	s_movk_i32 s0, 0x80
	s_movk_i32 s8, 0x1000
	v_bfrev_b32_e32 v122, 1
	v_and_b32_e32 v120, 63, v121
	v_cmp_gt_i32_e32 vcc, s0, v121
	v_mov_b32_e32 v123, 1.0
	v_mov_b32_e32 v168, 0
	v_mov_b32_e32 v124, 0
	v_mov_b32_e32 v125, 0
	s_and_saveexec_b64 s[0:1], vcc
	s_cbranch_execz .LBB0_306
	v_and_b32_e32 v2, 64, v121
	v_cmp_eq_u32_e32 vcc, 0, v2
	v_xor_b32_e32 v2, 63, v120
	v_readlane_b32 s6, v252, 3
	v_cndmask_b32_e32 v2, v2, v120, vcc
	v_readlane_b32 s7, v252, 4
	v_add_u32_e32 v6, s4, v2
	v_ashrrev_i32_e32 v2, 4, v121
	v_mov_b64_e32 v[4:5], s[6:7]
	v_and_b32_e32 v2, -4, v2
	v_mad_i64_i32 v[4:5], s[6:7], v6, s81, v[4:5]
	v_ashrrev_i32_e32 v3, 31, v2
	s_add_i32 s6, s16, s56
	v_lshl_add_u64 v[4:5], v[2:3], 1, v[4:5]
	v_add_u32_e32 v2, s6, v2
	v_ashrrev_i32_e32 v3, 31, v2
	v_readlane_b32 s40, v251, 19
	s_ashr_i32 s17, s16, 31
	v_lshlrev_b64 v[2:3], 2, v[2:3]
	v_readlane_b32 s44, v251, 23
	v_readlane_b32 s45, v251, 24
	v_readlane_b32 s46, v251, 25
	v_readlane_b32 s47, v251, 26
	v_lshl_add_u64 v[4:5], s[16:17], 1, v[4:5]
	v_lshl_add_u64 v[6:7], s[44:45], 0, v[2:3]
	v_lshl_add_u64 v[2:3], s[46:47], 0, v[2:3]
	global_load_dword v124, v[2:3], off
	v_add_co_u32_e32 v2, vcc, s8, v4
	global_load_dword v169, v[6:7], off
	s_nop 0
	v_addc_co_u32_e32 v3, vcc, 0, v5, vcc
	global_load_ushort v170, v[2:3], off
	global_load_ushort v171, v[2:3], off offset:16
	v_readlane_b32 s41, v251, 20
	v_readlane_b32 s42, v251, 21
	v_readlane_b32 s43, v251, 22
	v_readlane_b32 s48, v251, 27
	v_readlane_b32 s49, v251, 28
	v_readlane_b32 s50, v251, 29
	v_readlane_b32 s51, v251, 30
	v_readlane_b32 s52, v251, 31
	v_readlane_b32 s53, v251, 32
	v_readlane_b32 s54, v251, 33
	v_readlane_b32 s55, v251, 34
.LBB0_306:
	s_or_b64 exec, exec, s[0:1]
	s_lshl_b32 s6, s16, 7
	s_ashr_i32 s7, s6, 31
	v_readlane_b32 s40, v251, 19
	s_lshl_b64 s[0:1], s[6:7], 2
	v_readlane_b32 s42, v251, 21
	v_and_b32_e32 v118, 63, v167
	v_readlane_b32 s43, v251, 22
	s_add_u32 s0, s42, s0
	s_addc_u32 s1, s43, s1
	v_lshlrev_b32_e32 v130, 3, v118
	v_lshl_add_u64 v[2:3], s[0:1], 0, v[130:131]
	v_readlane_b32 s0, v255, 6
	v_readlane_b32 s54, v251, 33
	v_readlane_b32 s1, v255, 7
	s_movk_i32 s54, 0x1000
	v_ashrrev_i32_e32 v119, 6, v167
	v_lshl_add_u64 v[8:9], v[2:3], 0, s[0:1]
	v_add_co_u32_e32 v4, vcc, s54, v8
	s_movk_i32 s0, 0x3000
	s_nop 0
	v_addc_co_u32_e32 v5, vcc, 0, v9, vcc
	v_add_co_u32_e32 v6, vcc, s76, v8
	global_load_dwordx2 v[10:11], v[8:9], off
	global_load_dwordx2 v[2:3], v[8:9], off offset:2048
	v_addc_co_u32_e32 v7, vcc, 0, v9, vcc
	global_load_dwordx2 v[84:85], v[6:7], off offset:-4096
	global_load_dwordx2 v[12:13], v[4:5], off offset:2048
	s_nop 0
	global_load_dwordx2 v[4:5], v[6:7], off
	global_load_dwordx2 v[86:87], v[6:7], off offset:2048
	v_add_co_u32_e32 v6, vcc, s0, v8
	s_movk_i32 s0, 0x5000
	s_nop 0
	v_addc_co_u32_e32 v7, vcc, 0, v9, vcc
	v_add_co_u32_e32 v16, vcc, s88, v8
	v_lshl_add_u32 v22, v119, 3, s4
	s_nop 0
	v_addc_co_u32_e32 v17, vcc, 0, v9, vcc
	s_add_i32 s4, s3, s5
	v_add_co_u32_e32 v18, vcc, s0, v8
	s_add_i32 s0, s4, -1
	s_lshl_b64 s[6:7], s[6:7], 1
	v_readlane_b32 s8, v252, 3
	v_add_u32_e32 v23, -2, v22
	v_readlane_b32 s9, v252, 4
	s_add_u32 s6, s8, s6
	v_addc_co_u32_e32 v19, vcc, 0, v9, vcc
	s_addc_u32 s7, s9, s7
	v_lshlrev_b32_e32 v164, 2, v118
	v_mov_b32_e32 v165, v131
	v_max_i32_e32 v20, s3, v23
	global_load_dwordx2 v[14:15], v[16:17], off offset:-4096
	s_nop 0
	global_load_dwordx2 v[6:7], v[6:7], off offset:2048
	s_nop 0
	global_load_dwordx2 v[92:93], v[16:17], off
	s_nop 0
	global_load_dwordx2 v[16:17], v[16:17], off offset:2048
	s_nop 0
	global_load_dwordx2 v[8:9], v[18:19], off
	global_load_dwordx2 v[94:95], v[18:19], off offset:2048
	v_lshl_add_u64 v[18:19], s[6:7], 0, v[164:165]
	v_min_i32_e32 v20, s0, v20
	s_movk_i32 s1, 0x3800
	v_mad_i64_i32 v[20:21], s[6:7], v20, s1, v[18:19]
	v_add_u32_e32 v27, -1, v22
	global_load_dword v24, v[20:21], off
	global_load_dword v25, v[20:21], off offset:1024
	global_load_dword v26, v[20:21], off offset:2048
	v_max_i32_e32 v20, s3, v27
	v_min_i32_e32 v20, s0, v20
	v_mad_i64_i32 v[20:21], s[6:7], v20, s1, v[18:19]
	global_load_dword v28, v[20:21], off
	global_load_dword v29, v[20:21], off offset:1024
	global_load_dword v30, v[20:21], off offset:2048
	v_max_i32_e32 v20, s3, v22
	v_min_i32_e32 v20, s0, v20
	v_mad_i64_i32 v[20:21], s[6:7], v20, s1, v[18:19]
	v_add_u32_e32 v82, 1, v22
	global_load_dword v31, v[20:21], off
	global_load_dword v32, v[20:21], off offset:1024
	global_load_dword v33, v[20:21], off offset:2048
	v_max_i32_e32 v20, s3, v82
	v_min_i32_e32 v20, s0, v20
	v_mad_i64_i32 v[20:21], s[6:7], v20, s1, v[18:19]
	v_add_u32_e32 v90, 2, v22
	global_load_dword v83, v[20:21], off
	global_load_dword v88, v[20:21], off offset:1024
	global_load_dword v89, v[20:21], off offset:2048
	v_max_i32_e32 v20, s3, v90
	v_min_i32_e32 v20, s0, v20
	v_mad_i64_i32 v[20:21], s[6:7], v20, s1, v[18:19]
	v_add_u32_e32 v138, 3, v22
	global_load_dword v91, v[20:21], off
	global_load_dword v96, v[20:21], off offset:1024
	global_load_dword v97, v[20:21], off offset:2048
	v_max_i32_e32 v20, s3, v138
	v_min_i32_e32 v20, s0, v20
	v_mad_i64_i32 v[20:21], s[6:7], v20, s1, v[18:19]
	v_add_u32_e32 v142, 4, v22
	global_load_dword v139, v[20:21], off
	global_load_dword v140, v[20:21], off offset:1024
	global_load_dword v141, v[20:21], off offset:2048
	v_max_i32_e32 v20, s3, v142
	v_min_i32_e32 v20, s0, v20
	v_mad_i64_i32 v[20:21], s[6:7], v20, s1, v[18:19]
	v_add_u32_e32 v146, 5, v22
	global_load_dword v143, v[20:21], off
	global_load_dword v144, v[20:21], off offset:1024
	global_load_dword v145, v[20:21], off offset:2048
	v_max_i32_e32 v20, s3, v146
	v_min_i32_e32 v20, s0, v20
	v_mad_i64_i32 v[20:21], s[6:7], v20, s1, v[18:19]
	v_add_u32_e32 v150, 6, v22
	global_load_dword v147, v[20:21], off
	global_load_dword v148, v[20:21], off offset:1024
	global_load_dword v149, v[20:21], off offset:2048
	v_max_i32_e32 v20, s3, v150
	v_min_i32_e32 v20, s0, v20
	v_mad_i64_i32 v[20:21], s[6:7], v20, s1, v[18:19]
	v_add_u32_e32 v154, 7, v22
	global_load_dword v151, v[20:21], off
	global_load_dword v152, v[20:21], off offset:1024
	global_load_dword v153, v[20:21], off offset:2048
	v_max_i32_e32 v20, s3, v154
	v_min_i32_e32 v20, s0, v20
	v_mad_i64_i32 v[20:21], s[6:7], v20, s1, v[18:19]
	v_add_u32_e32 v158, 8, v22
	global_load_dword v155, v[20:21], off
	global_load_dword v156, v[20:21], off offset:1024
	global_load_dword v157, v[20:21], off offset:2048
	v_max_i32_e32 v20, s3, v158
	v_min_i32_e32 v20, s0, v20
	v_mad_i64_i32 v[18:19], s[0:1], v20, s1, v[18:19]
	global_load_dword v159, v[18:19], off
	global_load_dword v160, v[18:19], off offset:1024
	global_load_dword v161, v[18:19], off offset:2048
	v_readlane_b32 s46, v251, 25
	s_movk_i32 s81, 0x3800
	v_readlane_b32 s41, v251, 20
	v_readlane_b32 s44, v251, 23
	v_readlane_b32 s45, v251, 24
	v_readlane_b32 s47, v251, 26
	v_readlane_b32 s48, v251, 27
	v_readlane_b32 s49, v251, 28
	v_readlane_b32 s50, v251, 29
	v_readlane_b32 s51, v251, 30
	v_readlane_b32 s52, v251, 31
	v_readlane_b32 s53, v251, 32
	v_readlane_b32 s55, v251, 34
	s_waitcnt vmcnt(0)
	v_cmp_gt_i32_e32 vcc, 0x80, v167
	s_and_saveexec_b64 s[0:1], vcc
	s_cbranch_execz .Lgdn_gate_skip
	s_mov_b32 s100, 0x3fb8aa3b
	v_mul_f32_e32 v172, 0x3fb8aa3b, v169
	v_rndne_f32_e32 v174, v172
	v_lshlrev_b32_e32 v125, 16, v170
	v_fma_f32 v173, v169, s100, -v172
	v_fmac_f32_e32 v173, 0x32a5705f, v169
	v_sub_f32_e32 v172, v172, v174
	v_add_f32_e32 v172, v172, v173
	v_exp_f32_e32 v172, v172
	v_cvt_i32_f32_e32 v173, v174
	s_mov_b32 s100, 0xc2ce8ed0
	v_cmp_ngt_f32_e32 vcc, s100, v169
	s_mov_b32 s100, 0x42b17218
	v_ldexp_f32 v172, v172, v173
	v_lshlrev_b32_e32 v175, 16, v171
	v_cndmask_b32_e32 v172, 0, v172, vcc
	v_cmp_nlt_f32_e32 vcc, s100, v169
	v_mul_f32_e32 v122, 0xbfb8aa3b, v175
	s_nop 1
	v_cndmask_b32_e32 v123, v234, v172, vcc
.Lgdn_gate_skip:
	s_or_b64 exec, exec, s[0:1]
	v_cmp_le_i32_e32 vcc, s3, v23
	v_cmp_gt_i32_e64 s[0:1], s4, v23
	s_and_b64 vcc, vcc, s[0:1]
	s_nop 1
	v_cndmask_b32_e32 v18, 0, v24, vcc
	v_lshlrev_b32_e32 v116, 16, v18
	v_and_b32_e32 v117, 0xffff0000, v18
	v_cndmask_b32_e32 v18, 0, v25, vcc
	v_lshlrev_b32_e32 v114, 16, v18
	v_and_b32_e32 v115, 0xffff0000, v18
	v_cndmask_b32_e32 v18, 0, v26, vcc
	v_cmp_le_i32_e32 vcc, s3, v27
	v_cmp_gt_i32_e64 s[0:1], s4, v27
	s_and_b64 vcc, vcc, s[0:1]
	v_lshlrev_b32_e32 v126, 16, v18
	v_and_b32_e32 v127, 0xffff0000, v18
	v_cndmask_b32_e32 v18, 0, v28, vcc
	v_lshlrev_b32_e32 v112, 16, v18
	v_and_b32_e32 v113, 0xffff0000, v18
	v_cndmask_b32_e32 v18, 0, v29, vcc
	v_lshlrev_b32_e32 v110, 16, v18
	v_and_b32_e32 v111, 0xffff0000, v18
	v_cndmask_b32_e32 v18, 0, v30, vcc
	v_cmp_le_i32_e32 vcc, s3, v22
	v_cmp_gt_i32_e64 s[0:1], s4, v22
	s_and_b64 vcc, vcc, s[0:1]
	v_lshlrev_b32_e32 v128, 16, v18
	v_and_b32_e32 v129, 0xffff0000, v18
	v_cndmask_b32_e32 v18, 0, v31, vcc
	v_lshlrev_b32_e32 v108, 16, v18
	v_and_b32_e32 v109, 0xffff0000, v18
	v_cndmask_b32_e32 v18, 0, v32, vcc
	v_lshlrev_b32_e32 v106, 16, v18
	v_and_b32_e32 v107, 0xffff0000, v18
	v_cndmask_b32_e32 v18, 0, v33, vcc
	v_cmp_le_i32_e32 vcc, s3, v82
	v_cmp_gt_i32_e64 s[0:1], s4, v82
	s_and_b64 vcc, vcc, s[0:1]
	v_lshlrev_b32_e32 v132, 16, v18
	v_and_b32_e32 v133, 0xffff0000, v18
	v_cndmask_b32_e32 v18, 0, v83, vcc
	v_lshlrev_b32_e32 v104, 16, v18
	v_and_b32_e32 v105, 0xffff0000, v18
	v_cndmask_b32_e32 v18, 0, v88, vcc
	v_lshlrev_b32_e32 v102, 16, v18
	v_and_b32_e32 v103, 0xffff0000, v18
	v_cndmask_b32_e32 v18, 0, v89, vcc
	v_cmp_le_i32_e32 vcc, s3, v90
	v_cmp_gt_i32_e64 s[0:1], s4, v90
	s_and_b64 vcc, vcc, s[0:1]
	v_lshlrev_b32_e32 v134, 16, v18
	v_and_b32_e32 v135, 0xffff0000, v18
	v_cndmask_b32_e32 v18, 0, v91, vcc
	v_lshlrev_b32_e32 v100, 16, v18
	v_and_b32_e32 v101, 0xffff0000, v18
	v_cndmask_b32_e32 v18, 0, v96, vcc
	v_lshlrev_b32_e32 v98, 16, v18
	v_and_b32_e32 v99, 0xffff0000, v18
	v_cndmask_b32_e32 v18, 0, v97, vcc
	v_cmp_le_i32_e32 vcc, s3, v138
	v_cmp_gt_i32_e64 s[0:1], s4, v138
	s_and_b64 vcc, vcc, s[0:1]
	v_lshlrev_b32_e32 v136, 16, v18
	v_and_b32_e32 v137, 0xffff0000, v18
	v_cndmask_b32_e32 v18, 0, v139, vcc
	v_lshlrev_b32_e32 v96, 16, v18
	v_and_b32_e32 v97, 0xffff0000, v18
	v_cndmask_b32_e32 v18, 0, v140, vcc
	v_lshlrev_b32_e32 v90, 16, v18
	v_and_b32_e32 v91, 0xffff0000, v18
	v_cndmask_b32_e32 v18, 0, v141, vcc
	v_cmp_le_i32_e32 vcc, s3, v142
	v_cmp_gt_i32_e64 s[0:1], s4, v142
	s_and_b64 vcc, vcc, s[0:1]
	v_lshlrev_b32_e32 v138, 16, v18
	v_and_b32_e32 v139, 0xffff0000, v18
	v_cndmask_b32_e32 v18, 0, v143, vcc
	v_lshlrev_b32_e32 v88, 16, v18
	v_and_b32_e32 v89, 0xffff0000, v18
	v_cndmask_b32_e32 v18, 0, v144, vcc
	v_lshlrev_b32_e32 v32, 16, v18
	v_and_b32_e32 v33, 0xffff0000, v18
	v_cndmask_b32_e32 v18, 0, v145, vcc
	v_cmp_le_i32_e32 vcc, s3, v146
	v_cmp_gt_i32_e64 s[0:1], s4, v146
	s_and_b64 vcc, vcc, s[0:1]
	v_lshlrev_b32_e32 v140, 16, v18
	v_and_b32_e32 v141, 0xffff0000, v18
	v_cndmask_b32_e32 v18, 0, v147, vcc
	v_cndmask_b32_e32 v19, 0, v148, vcc
	v_cndmask_b32_e32 v20, 0, v149, vcc
	v_cmp_le_i32_e32 vcc, s3, v150
	v_cmp_gt_i32_e64 s[0:1], s4, v150
	s_and_b64 vcc, vcc, s[0:1]
	v_lshlrev_b32_e32 v142, 16, v20
	v_and_b32_e32 v143, 0xffff0000, v20
	v_cndmask_b32_e32 v20, 0, v151, vcc
	v_pk_mul_f32 v[150:151], v[86:87], v[128:129]
	v_cndmask_b32_e32 v21, 0, v152, vcc
	v_pk_fma_f32 v[126:127], v[84:85], v[126:127], v[150:151]
	v_cndmask_b32_e32 v22, 0, v153, vcc
	v_pk_fma_f32 v[126:127], v[92:93], v[132:133], v[126:127]
	v_pk_mul_f32 v[152:153], v[86:87], v[132:133]
	v_pk_fma_f32 v[126:127], v[94:95], v[134:135], v[126:127]
	v_pk_fma_f32 v[128:129], v[84:85], v[128:129], v[152:153]
	v_mul_f32_e32 v150, 0xbfb8aa3b, v126
	v_mul_f32_e32 v151, 0xbfb8aa3b, v127
	v_exp_f32_e32 v150, v150
	v_exp_f32_e32 v151, v151
	v_pk_fma_f32 v[128:129], v[92:93], v[134:135], v[128:129]
	v_cmp_le_i32_e32 vcc, s3, v154
	v_pk_fma_f32 v[128:129], v[94:95], v[136:137], v[128:129]
	v_add_f32_e32 v150, 1.0, v150
	v_mul_f32_e32 v152, 0xbfb8aa3b, v128
	v_mul_f32_e32 v153, 0xbfb8aa3b, v129
	v_add_f32_e32 v151, 1.0, v151
	v_exp_f32_e32 v152, v152
	v_exp_f32_e32 v153, v153
	v_rcp_f32_e32 v150, v150
	v_rcp_f32_e32 v151, v151
	v_add_f32_e32 v152, 1.0, v152
	v_add_f32_e32 v153, 1.0, v153
	v_rcp_f32_e32 v152, v152
	v_rcp_f32_e32 v153, v153
	v_pk_mul_f32 v[126:127], v[126:127], v[150:151]
	v_pk_mul_f32 v[150:151], v[86:87], v[134:135]
	v_cmp_gt_i32_e64 s[0:1], s4, v154
	v_pk_fma_f32 v[132:133], v[84:85], v[132:133], v[150:151]
	v_lshlrev_b32_e32 v154, 12, v119
	v_pk_fma_f32 v[132:133], v[92:93], v[136:137], v[132:133]
	v_add3_u32 v130, 0, v154, v130
	v_pk_fma_f32 v[132:133], v[94:95], v[138:139], v[132:133]
	v_pk_mul_f32 v[128:129], v[128:129], v[152:153]
	v_mul_f32_e32 v150, 0xbfb8aa3b, v132
	v_mul_f32_e32 v151, 0xbfb8aa3b, v133
	v_exp_f32_e32 v150, v150
	v_exp_f32_e32 v151, v151
	ds_write2st64_b64 v130, v[126:127], v[128:129] offset0:68 offset1:69
	v_pk_mul_f32 v[128:129], v[86:87], v[136:137]
	v_add_f32_e32 v126, 1.0, v150
	v_pk_fma_f32 v[128:129], v[84:85], v[134:135], v[128:129]
	v_add_f32_e32 v127, 1.0, v151
	v_pk_fma_f32 v[128:129], v[92:93], v[138:139], v[128:129]
	v_rcp_f32_e32 v126, v126
	v_pk_fma_f32 v[128:129], v[94:95], v[140:141], v[128:129]
	v_rcp_f32_e32 v127, v127
	v_mul_f32_e32 v134, 0xbfb8aa3b, v128
	v_mul_f32_e32 v135, 0xbfb8aa3b, v129
	v_exp_f32_e32 v134, v134
	v_exp_f32_e32 v135, v135
	v_pk_mul_f32 v[126:127], v[132:133], v[126:127]
	v_pk_mul_f32 v[150:151], v[86:87], v[140:141]
	v_add_f32_e32 v132, 1.0, v134
	v_add_f32_e32 v133, 1.0, v135
	v_pk_mul_f32 v[134:135], v[86:87], v[138:139]
	v_rcp_f32_e32 v132, v132
	v_pk_fma_f32 v[134:135], v[84:85], v[136:137], v[134:135]
	v_rcp_f32_e32 v133, v133
	v_pk_fma_f32 v[134:135], v[92:93], v[140:141], v[134:135]
	s_and_b64 vcc, vcc, s[0:1]
	v_pk_fma_f32 v[134:135], v[94:95], v[142:143], v[134:135]
	v_pk_fma_f32 v[138:139], v[84:85], v[138:139], v[150:151]
	v_mul_f32_e32 v136, 0xbfb8aa3b, v134
	v_mul_f32_e32 v137, 0xbfb8aa3b, v135
	v_exp_f32_e32 v136, v136
	v_exp_f32_e32 v137, v137
	v_lshlrev_b32_e32 v144, 16, v22
	v_and_b32_e32 v145, 0xffff0000, v22
	v_cndmask_b32_e32 v22, 0, v155, vcc
	v_cndmask_b32_e32 v23, 0, v156, vcc
	v_cndmask_b32_e32 v24, 0, v157, vcc
	v_cmp_le_i32_e32 vcc, s3, v158
	v_cmp_gt_i32_e64 s[0:1], s4, v158
	v_pk_fma_f32 v[138:139], v[92:93], v[142:143], v[138:139]
	s_and_b64 vcc, vcc, s[0:1]
	v_pk_fma_f32 v[138:139], v[94:95], v[144:145], v[138:139]
	v_pk_mul_f32 v[128:129], v[128:129], v[132:133]
	v_pk_mul_f32 v[132:133], v[86:87], v[142:143]
	v_pk_mul_f32 v[86:87], v[86:87], v[144:145]
	v_lshlrev_b32_e32 v146, 16, v24
	v_and_b32_e32 v147, 0xffff0000, v24
	v_cndmask_b32_e32 v149, 0, v161, vcc
	v_mul_f32_e32 v150, 0xbfb8aa3b, v138
	v_mul_f32_e32 v151, 0xbfb8aa3b, v139
	v_pk_fma_f32 v[132:133], v[84:85], v[140:141], v[132:133]
	v_pk_fma_f32 v[84:85], v[84:85], v[142:143], v[86:87]
	v_lshlrev_b32_e32 v148, 16, v149
	v_and_b32_e32 v149, 0xffff0000, v149
	v_add_f32_e32 v136, 1.0, v136
	v_add_f32_e32 v137, 1.0, v137
	v_exp_f32_e32 v150, v150
	v_exp_f32_e32 v151, v151
	v_pk_fma_f32 v[132:133], v[92:93], v[144:145], v[132:133]
	v_pk_fma_f32 v[84:85], v[92:93], v[146:147], v[84:85]
	v_rcp_f32_e32 v136, v136
	v_rcp_f32_e32 v137, v137
	v_pk_fma_f32 v[132:133], v[94:95], v[146:147], v[132:133]
	v_pk_fma_f32 v[84:85], v[94:95], v[148:149], v[84:85]
	v_pk_mul_f32 v[94:95], v[12:13], v[112:113]
	v_add_f32_e32 v150, 1.0, v150
	v_pk_fma_f32 v[94:95], v[10:11], v[116:117], v[94:95]
	v_add_f32_e32 v151, 1.0, v151
	v_pk_fma_f32 v[94:95], v[14:15], v[108:109], v[94:95]
	v_mul_f32_e32 v86, 0xbfb8aa3b, v84
	v_pk_fma_f32 v[94:95], v[16:17], v[104:105], v[94:95]
	v_rcp_f32_e32 v150, v150
	v_rcp_f32_e32 v151, v151
	ds_write2st64_b64 v130, v[126:127], v[128:129] offset0:70 offset1:71
	v_pk_mul_f32 v[126:127], v[134:135], v[136:137]
	v_mul_f32_e32 v134, 0xbfb8aa3b, v132
	v_mul_f32_e32 v135, 0xbfb8aa3b, v133
	v_exp_f32_e32 v92, v86
	v_mul_f32_e32 v86, 0xbfb8aa3b, v85
	v_mul_f32_e32 v116, 0xbfb8aa3b, v94
	v_mul_f32_e32 v117, 0xbfb8aa3b, v95
	v_exp_f32_e32 v134, v134
	v_exp_f32_e32 v135, v135
	v_exp_f32_e32 v93, v86
	v_exp_f32_e32 v116, v116
	v_exp_f32_e32 v117, v117
	v_pk_mul_f32 v[128:129], v[138:139], v[150:151]
	ds_write2st64_b64 v130, v[126:127], v[128:129] offset0:72 offset1:73
	v_add_f32_e32 v126, 1.0, v134
	v_add_f32_e32 v127, 1.0, v135
	v_add_f32_e32 v92, 1.0, v92
	v_add_f32_e32 v93, 1.0, v93
	v_add_f32_e32 v116, 1.0, v116
	v_add_f32_e32 v117, 1.0, v117
	v_rcp_f32_e32 v126, v126
	v_rcp_f32_e32 v127, v127
	v_rcp_f32_e32 v92, v92
	v_rcp_f32_e32 v93, v93
	v_rcp_f32_e32 v116, v116
	v_rcp_f32_e32 v117, v117
	v_pk_mul_f32 v[86:87], v[132:133], v[126:127]
	v_pk_mul_f32 v[84:85], v[84:85], v[92:93]
	ds_write2st64_b64 v130, v[86:87], v[84:85] offset0:74 offset1:75
	v_pk_mul_f32 v[92:93], v[94:95], v[116:117]
	s_movk_i32 s0, 0x880
	v_mul_f32_e32 v84, v93, v93
	v_pk_fma_f32 v[116:117], v[92:93], v[92:93], v[84:85] op_sel_hi:[1,1,0]
	v_pk_mul_f32 v[84:85], v[4:5], v[110:111]
	v_mul_lo_u32 v86, v119, s0
	v_pk_fma_f32 v[84:85], v[2:3], v[114:115], v[84:85]
	v_add3_u32 v114, 0, v164, v86
	v_pk_fma_f32 v[84:85], v[6:7], v[106:107], v[84:85]
	v_pk_mul_f32 v[128:129], v[12:13], v[104:105]
	v_pk_fma_f32 v[84:85], v[8:9], v[102:103], v[84:85]
	v_pk_mul_f32 v[134:135], v[12:13], v[100:101]
	v_mul_f32_e32 v87, 0xbfb8aa3b, v84
	v_mul_f32_e32 v94, 0xbfb8aa3b, v85
	v_exp_f32_e32 v87, v87
	v_exp_f32_e32 v94, v94
	v_pk_mul_f32 v[138:139], v[12:13], v[96:97]
	v_lshlrev_b32_e32 v26, 16, v18
	v_add_f32_e32 v86, 1.0, v87
	v_add_f32_e32 v87, 1.0, v94
	v_pk_mul_f32 v[94:95], v[12:13], v[108:109]
	v_rcp_f32_e32 v86, v86
	v_pk_fma_f32 v[94:95], v[10:11], v[112:113], v[94:95]
	v_rcp_f32_e32 v87, v87
	v_pk_fma_f32 v[94:95], v[14:15], v[104:105], v[94:95]
	v_pk_fma_f32 v[108:109], v[10:11], v[108:109], v[128:129]
	v_pk_fma_f32 v[94:95], v[16:17], v[100:101], v[94:95]
	v_pk_mul_f32 v[84:85], v[84:85], v[86:87]
	v_mul_f32_e32 v112, 0xbfb8aa3b, v94
	v_mul_f32_e32 v113, 0xbfb8aa3b, v95
	v_exp_f32_e32 v112, v112
	v_exp_f32_e32 v113, v113
	v_mul_f32_e32 v86, v85, v85
	v_pk_fma_f32 v[126:127], v[84:85], v[84:85], v[86:87] op_sel_hi:[1,1,0]
	v_add_f32_e32 v112, 1.0, v112
	v_add_f32_e32 v113, 1.0, v113
	v_rcp_f32_e32 v112, v112
	v_rcp_f32_e32 v113, v113
	v_pk_fma_f32 v[108:109], v[14:15], v[100:101], v[108:109]
	v_pk_fma_f32 v[104:105], v[10:11], v[104:105], v[134:135]
	v_pk_fma_f32 v[108:109], v[16:17], v[96:97], v[108:109]
	v_pk_mul_f32 v[112:113], v[94:95], v[112:113]
	v_pk_mul_f32 v[94:95], v[4:5], v[106:107]
	v_mul_f32_e32 v86, v113, v113
	v_pk_fma_f32 v[94:95], v[2:3], v[110:111], v[94:95]
	v_pk_fma_f32 v[104:105], v[14:15], v[96:97], v[104:105]
	v_pk_fma_f32 v[94:95], v[6:7], v[102:103], v[94:95]
	v_pk_fma_f32 v[104:105], v[16:17], v[88:89], v[104:105]
	v_pk_fma_f32 v[94:95], v[8:9], v[98:99], v[94:95]
	v_pk_fma_f32 v[100:101], v[10:11], v[100:101], v[138:139]
	v_mul_f32_e32 v87, 0xbfb8aa3b, v94
	v_exp_f32_e32 v87, v87
	v_mul_f32_e32 v110, 0xbfb8aa3b, v95
	v_exp_f32_e32 v115, v110
	v_and_b32_e32 v27, 0xffff0000, v18
	v_pk_fma_f32 v[110:111], v[112:113], v[112:113], v[86:87] op_sel_hi:[1,1,0]
	v_add_f32_e32 v86, 1.0, v87
	v_mul_f32_e32 v111, 0xbfb8aa3b, v108
	v_add_f32_e32 v87, 1.0, v115
	v_exp_f32_e32 v111, v111
	v_mul_f32_e32 v115, 0xbfb8aa3b, v109
	v_exp_f32_e32 v115, v115
	v_rcp_f32_e32 v86, v86
	v_add_f32_e32 v111, 1.0, v111
	v_rcp_f32_e32 v128, v111
	v_add_f32_e32 v111, 1.0, v115
	v_rcp_f32_e32 v129, v111
	v_rcp_f32_e32 v87, v87
	v_mul_f32_e32 v115, 0xbfb8aa3b, v105
	v_exp_f32_e32 v115, v115
	v_pk_mul_f32 v[108:109], v[108:109], v[128:129]
	v_pk_mul_f32 v[128:129], v[4:5], v[102:103]
	v_pk_mul_f32 v[86:87], v[94:95], v[86:87]
	v_pk_fma_f32 v[106:107], v[2:3], v[106:107], v[128:129]
	v_mul_f32_e32 v94, v87, v87
	v_pk_fma_f32 v[106:107], v[6:7], v[98:99], v[106:107]
	v_pk_fma_f32 v[132:133], v[86:87], v[86:87], v[94:95] op_sel_hi:[1,1,0]
	v_pk_fma_f32 v[106:107], v[8:9], v[90:91], v[106:107]
	v_mul_f32_e32 v94, v109, v109
	v_mul_f32_e32 v95, 0xbfb8aa3b, v106
	v_mul_f32_e32 v111, 0xbfb8aa3b, v107
	v_exp_f32_e32 v95, v95
	v_exp_f32_e32 v111, v111
	v_pk_fma_f32 v[100:101], v[14:15], v[88:89], v[100:101]
	v_lshlrev_b32_e32 v18, 16, v19
	v_pk_fma_f32 v[128:129], v[108:109], v[108:109], v[94:95] op_sel_hi:[1,1,0]
	v_add_f32_e32 v94, 1.0, v95
	v_add_f32_e32 v95, 1.0, v111
	v_mul_f32_e32 v111, 0xbfb8aa3b, v104
	v_exp_f32_e32 v111, v111
	v_rcp_f32_e32 v94, v94
	v_rcp_f32_e32 v95, v95
	v_pk_fma_f32 v[138:139], v[16:17], v[26:27], v[100:101]
	v_add_f32_e32 v111, 1.0, v111
	v_rcp_f32_e32 v134, v111
	v_add_f32_e32 v111, 1.0, v115
	v_rcp_f32_e32 v135, v111
	v_pk_mul_f32 v[94:95], v[106:107], v[94:95]
	v_mul_f32_e32 v100, 0xbfb8aa3b, v138
	v_mul_f32_e32 v106, v95, v95
	v_pk_mul_f32 v[104:105], v[104:105], v[134:135]
	v_pk_mul_f32 v[134:135], v[4:5], v[98:99]
	v_pk_fma_f32 v[136:137], v[94:95], v[94:95], v[106:107] op_sel_hi:[1,1,0]
	v_pk_fma_f32 v[102:103], v[2:3], v[102:103], v[134:135]
	v_exp_f32_e32 v100, v100
	v_pk_fma_f32 v[102:103], v[6:7], v[90:91], v[102:103]
	v_mul_f32_e32 v101, 0xbfb8aa3b, v139
	v_pk_fma_f32 v[102:103], v[8:9], v[32:33], v[102:103]
	v_exp_f32_e32 v101, v101
	v_mul_f32_e32 v107, 0xbfb8aa3b, v102
	v_mul_f32_e32 v111, 0xbfb8aa3b, v103
	v_exp_f32_e32 v107, v107
	v_exp_f32_e32 v111, v111
	v_mul_f32_e32 v106, v105, v105
	v_add_f32_e32 v100, 1.0, v100
	v_pk_fma_f32 v[134:135], v[104:105], v[104:105], v[106:107] op_sel_hi:[1,1,0]
	v_add_f32_e32 v106, 1.0, v107
	v_add_f32_e32 v107, 1.0, v111
	v_rcp_f32_e32 v140, v100
	v_add_f32_e32 v100, 1.0, v101
	v_rcp_f32_e32 v106, v106
	v_rcp_f32_e32 v107, v107
	v_rcp_f32_e32 v141, v100
	v_and_b32_e32 v19, 0xffff0000, v19
	v_lshlrev_b32_e32 v28, 16, v20
	v_pk_mul_f32 v[100:101], v[102:103], v[106:107]
	v_pk_mul_f32 v[106:107], v[138:139], v[140:141]
	v_pk_mul_f32 v[138:139], v[4:5], v[90:91]
	v_mul_f32_e32 v102, v101, v101
	v_pk_fma_f32 v[98:99], v[2:3], v[98:99], v[138:139]
	v_pk_fma_f32 v[102:103], v[100:101], v[100:101], v[102:103] op_sel_hi:[1,1,0]
	v_pk_fma_f32 v[98:99], v[6:7], v[32:33], v[98:99]
	v_mul_f32_e32 v130, v107, v107
	v_pk_fma_f32 v[98:99], v[8:9], v[18:19], v[98:99]
	v_pk_fma_f32 v[138:139], v[106:107], v[106:107], v[130:131] op_sel_hi:[1,1,0]
	v_mul_f32_e32 v103, 0xbfb8aa3b, v98
	v_exp_f32_e32 v103, v103
	v_mul_f32_e32 v111, 0xbfb8aa3b, v99
	v_exp_f32_e32 v111, v111
	v_permlane32_swap_b32_e32 v116, v138
	v_add_f32_e32 v103, 1.0, v103
	v_rcp_f32_e32 v140, v103
	v_add_f32_e32 v103, 1.0, v111
	v_rcp_f32_e32 v141, v103
	v_add_f32_e32 v103, v116, v138
	v_pk_mul_f32 v[138:139], v[12:13], v[88:89]
	v_and_b32_e32 v29, 0xffff0000, v20
	v_pk_fma_f32 v[96:97], v[10:11], v[96:97], v[138:139]
	v_pk_mul_f32 v[98:99], v[98:99], v[140:141]
	v_pk_fma_f32 v[96:97], v[14:15], v[26:27], v[96:97]
	v_mul_f32_e32 v116, v99, v99
	v_pk_fma_f32 v[96:97], v[16:17], v[28:29], v[96:97]
	v_pk_fma_f32 v[116:117], v[98:99], v[98:99], v[116:117] op_sel_hi:[1,1,0]
	v_mul_f32_e32 v111, 0xbfb8aa3b, v96
	v_exp_f32_e32 v111, v111
	v_mul_f32_e32 v115, 0xbfb8aa3b, v97
	v_exp_f32_e32 v115, v115
	v_permlane32_swap_b32_e32 v126, v116
	v_add_f32_e32 v111, 1.0, v111
	v_rcp_f32_e32 v138, v111
	v_add_f32_e32 v111, 1.0, v115
	v_add_f32_e32 v115, v126, v116
	v_pk_mul_f32 v[126:127], v[4:5], v[32:33]
	v_rcp_f32_e32 v139, v111
	v_pk_fma_f32 v[90:91], v[2:3], v[90:91], v[126:127]
	v_lshlrev_b32_e32 v20, 16, v21
	v_and_b32_e32 v21, 0xffff0000, v21
	v_pk_fma_f32 v[90:91], v[6:7], v[18:19], v[90:91]
	v_pk_mul_f32 v[96:97], v[96:97], v[138:139]
	v_pk_fma_f32 v[90:91], v[8:9], v[20:21], v[90:91]
	v_mul_f32_e32 v116, v97, v97
	v_mul_f32_e32 v111, 0xbfb8aa3b, v90
	v_exp_f32_e32 v111, v111
	v_mul_f32_e32 v117, 0xbfb8aa3b, v91
	v_exp_f32_e32 v127, v117
	v_pk_fma_f32 v[116:117], v[96:97], v[96:97], v[116:117] op_sel_hi:[1,1,0]
	v_add_f32_e32 v111, 1.0, v111
	s_nop 0
	v_permlane32_swap_b32_e32 v110, v116
	v_add_f32_e32 v129, v110, v116
	v_pk_mul_f32 v[116:117], v[12:13], v[26:27]
	v_rcp_f32_e32 v126, v111
	v_add_f32_e32 v111, 1.0, v127
	v_pk_fma_f32 v[88:89], v[10:11], v[88:89], v[116:117]
	v_pk_mul_f32 v[12:13], v[12:13], v[28:29]
	v_lshlrev_b32_e32 v30, 16, v22
	v_and_b32_e32 v31, 0xffff0000, v22
	v_cndmask_b32_e32 v24, 0, v159, vcc
	v_rcp_f32_e32 v127, v111
	v_pk_fma_f32 v[88:89], v[14:15], v[28:29], v[88:89]
	v_pk_fma_f32 v[10:11], v[10:11], v[26:27], v[12:13]
	v_lshlrev_b32_e32 v82, 16, v24
	v_and_b32_e32 v83, 0xffff0000, v24
	v_pk_fma_f32 v[88:89], v[16:17], v[30:31], v[88:89]
	v_pk_fma_f32 v[10:11], v[14:15], v[30:31], v[10:11]
	v_mul_f32_e32 v111, 0xbfb8aa3b, v88
	v_pk_fma_f32 v[10:11], v[16:17], v[82:83], v[10:11]
	v_exp_f32_e32 v116, v111
	v_mul_f32_e32 v111, 0xbfb8aa3b, v89
	v_mul_f32_e32 v12, 0xbfb8aa3b, v10
	v_mul_f32_e32 v13, 0xbfb8aa3b, v11
	v_pk_mul_f32 v[90:91], v[90:91], v[126:127]
	v_exp_f32_e32 v117, v111
	v_exp_f32_e32 v12, v12
	v_exp_f32_e32 v13, v13
	v_mul_f32_e32 v110, v91, v91
	v_pk_fma_f32 v[110:111], v[90:91], v[90:91], v[110:111] op_sel_hi:[1,1,0]
	v_add_f32_e32 v12, 1.0, v12
	v_add_f32_e32 v111, 1.0, v116
	v_rcp_f32_e32 v116, v111
	v_add_f32_e32 v111, 1.0, v117
	v_add_f32_e32 v13, 1.0, v13
	v_rcp_f32_e32 v117, v111
	v_rcp_f32_e32 v12, v12
	v_rcp_f32_e32 v13, v13
	v_permlane32_swap_b32_e32 v132, v110
	v_pk_mul_f32 v[88:89], v[88:89], v[116:117]
	v_pk_mul_f32 v[10:11], v[10:11], v[12:13]
	v_add_f32_e32 v126, v132, v110
	v_mul_f32_e32 v110, v89, v89
	v_mul_f32_e32 v12, v11, v11
	v_pk_fma_f32 v[110:111], v[88:89], v[88:89], v[110:111] op_sel_hi:[1,1,0]
	v_pk_fma_f32 v[12:13], v[10:11], v[10:11], v[12:13] op_sel_hi:[1,1,0]
	s_nop 0
	v_permlane32_swap_b32_e32 v128, v110
	v_pk_mul_f32 v[116:117], v[4:5], v[18:19]
	v_permlane32_swap_b32_e32 v134, v12
	v_pk_fma_f32 v[32:33], v[2:3], v[32:33], v[116:117]
	v_add_f32_e32 v117, v128, v110
	v_add_f32_e32 v12, v134, v12
	v_and_b32_e32 v142, 8, v167
	v_permlane16_swap_b32_e32 v103, v117
	v_permlane16_swap_b32_e32 v129, v12
	v_cndmask_b32_e32 v25, 0, v160, vcc
	v_add_f32_e32 v103, v103, v117
	v_add_f32_e32 v12, v129, v12
	v_cmp_eq_u32_e32 vcc, 0, v142
	v_pk_mul_f32 v[4:5], v[4:5], v[20:21]
	v_lshlrev_b32_e32 v22, 16, v23
	v_cndmask_b32_e32 v13, v12, v103, vcc
	v_cndmask_b32_e32 v12, v103, v12, vcc
	v_and_b32_e32 v23, 0xffff0000, v23
	v_pk_fma_f32 v[2:3], v[2:3], v[18:19], v[4:5]
	v_add_f32_dpp v12, v12, v13 row_ror:8 row_mask:0xf bank_mask:0xf bound_ctrl:1
	v_lshlrev_b32_e32 v24, 16, v25
	v_and_b32_e32 v25, 0xffff0000, v25
	v_add_f32_dpp v12, v12, v12 row_half_mirror row_mask:0xf bank_mask:0xf bound_ctrl:1
	v_pk_fma_f32 v[2:3], v[6:7], v[22:23], v[2:3]
	v_pk_fma_f32 v[32:33], v[6:7], v[20:21], v[32:33]
	v_add_f32_dpp v12, v12, v12 quad_perm:[1,0,3,2] row_mask:0xf bank_mask:0xf bound_ctrl:1
	v_pk_fma_f32 v[2:3], v[8:9], v[24:25], v[2:3]
	v_pk_fma_f32 v[32:33], v[8:9], v[22:23], v[32:33]
	v_add_f32_dpp v12, v12, v12 quad_perm:[2,3,0,1] row_mask:0xf bank_mask:0xf bound_ctrl:1
	v_mul_f32_e32 v4, 0xbfb8aa3b, v2
	v_readlane_b32 s0, v12, 0
	v_readlane_b32 s1, v12, 8
	v_readlane_b32 s3, v12, 16
	v_add_f32_e32 v13, s0, v1
	v_rsq_f32_e32 v13, v13
	v_readlane_b32 s4, v12, 24
	v_readlane_b32 s5, v12, 32
	v_readlane_b32 s6, v12, 40
	v_readlane_b32 s7, v12, 48
	v_readlane_b32 s0, v12, 56
	v_add_f32_e32 v12, s1, v1
	v_rsq_f32_e32 v15, v12
	v_mul_f32_e32 v12, 0x3db504f3, v13
	v_pk_mul_f32 v[12:13], v[92:93], v[12:13] op_sel_hi:[1,0]
	v_mul_f32_e32 v111, 0xbfb8aa3b, v32
	v_cvt_pk_bf16_f32 v16, v12, v13
	v_mul_f32_e32 v12, 0x3db504f3, v15
	v_pk_mul_f32 v[12:13], v[112:113], v[12:13] op_sel_hi:[1,0]
	v_add_u32_e32 v15, 0x4400, v114
	v_cvt_pk_bf16_f32 v12, v12, v13
	v_add_f32_e32 v13, s3, v1
	v_rsq_f32_e32 v13, v13
	ds_write2_b32 v15, v16, v12 offset1:68
	v_add_f32_e32 v12, s4, v1
	v_rsq_f32_e32 v16, v12
	v_mul_f32_e32 v12, 0x3db504f3, v13
	v_pk_mul_f32 v[12:13], v[108:109], v[12:13] op_sel_hi:[1,0]
	v_mul_f32_e32 v116, 0xbfb8aa3b, v33
	v_cvt_pk_bf16_f32 v17, v12, v13
	v_mul_f32_e32 v12, 0x3db504f3, v16
	v_pk_mul_f32 v[12:13], v[104:105], v[12:13] op_sel_hi:[1,0]
	v_exp_f32_e32 v5, v4
	v_cvt_pk_bf16_f32 v12, v12, v13
	v_add_f32_e32 v13, s5, v1
	v_rsq_f32_e32 v13, v13
	ds_write2_b32 v15, v17, v12 offset0:136 offset1:204
	v_add_f32_e32 v12, s6, v1
	v_rsq_f32_e32 v15, v12
	v_mul_f32_e32 v12, 0x3db504f3, v13
	v_pk_mul_f32 v[12:13], v[106:107], v[12:13] op_sel_hi:[1,0]
	v_add_u32_e32 v17, 0x4800, v114
	v_cvt_pk_bf16_f32 v16, v12, v13
	v_mul_f32_e32 v12, 0x3db504f3, v15
	v_add_f32_e32 v15, s7, v1
	v_rsq_f32_e32 v15, v15
	v_pk_mul_f32 v[12:13], v[96:97], v[12:13] op_sel_hi:[1,0]
	v_mul_f32_e32 v4, 0xbfb8aa3b, v3
	v_cvt_pk_bf16_f32 v12, v12, v13
	v_exp_f32_e32 v111, v111
	v_exp_f32_e32 v116, v116
	ds_write2_b32 v17, v16, v12 offset0:16 offset1:84
	v_mul_f32_e32 v12, 0x3db504f3, v15
	v_exp_f32_e32 v7, v4
	v_pk_mul_f32 v[12:13], v[88:89], v[12:13] op_sel_hi:[1,0]
	v_add_f32_e32 v5, 1.0, v5
	v_cvt_pk_bf16_f32 v12, v12, v13
	v_add_f32_e32 v13, s0, v1
	v_rsq_f32_e32 v13, v13
	v_add_f32_e32 v110, 1.0, v111
	v_add_f32_e32 v111, 1.0, v116
	v_rcp_f32_e32 v6, v5
	v_add_f32_e32 v5, 1.0, v7
	v_rcp_f32_e32 v110, v110
	v_rcp_f32_e32 v111, v111
	v_rcp_f32_e32 v7, v5
	v_mul_f32_e32 v4, 0x3db504f3, v13
	v_pk_mul_f32 v[4:5], v[10:11], v[4:5] op_sel_hi:[1,0]
	v_pk_mul_f32 v[32:33], v[32:33], v[110:111]
	v_cvt_pk_bf16_f32 v4, v4, v5
	v_pk_mul_f32 v[2:3], v[2:3], v[6:7]
	v_mul_f32_e32 v110, v33, v33
	ds_write2_b32 v17, v12, v4 offset0:152 offset1:220
	v_mul_f32_e32 v4, v3, v3
	v_pk_fma_f32 v[110:111], v[32:33], v[32:33], v[110:111] op_sel_hi:[1,1,0]
	v_pk_fma_f32 v[4:5], v[2:3], v[2:3], v[4:5] op_sel_hi:[1,1,0]
	s_nop 0
	v_permlane32_swap_b32_e32 v136, v110
	v_permlane32_swap_b32_e32 v102, v4
	v_add_f32_e32 v14, v136, v110
	v_add_f32_e32 v4, v102, v4
	s_nop 0
	v_permlane16_swap_b32_e32 v115, v14
	v_permlane16_swap_b32_e32 v126, v4
	v_add_f32_e32 v14, v115, v14
	v_add_f32_e32 v4, v126, v4
	v_cndmask_b32_e32 v5, v4, v14, vcc
	v_cndmask_b32_e32 v4, v14, v4, vcc
	s_add_i32 s46, s2, 0x100
	s_cmpk_gt_i32 s2, 0x37f
	v_add_f32_dpp v4, v4, v5 row_ror:8 row_mask:0xf bank_mask:0xf bound_ctrl:1
	v_add_u32_e32 v8, 0x400, v114
	s_cselect_b64 s[36:37], -1, 0
	v_add_f32_dpp v4, v4, v4 row_half_mirror row_mask:0xf bank_mask:0xf bound_ctrl:1
	s_cmpk_lt_i32 s2, 0x380
	s_nop 0
	v_add_f32_dpp v4, v4, v4 quad_perm:[1,0,3,2] row_mask:0xf bank_mask:0xf bound_ctrl:1
	s_nop 1
	v_add_f32_dpp v5, v4, v4 quad_perm:[2,3,0,1] row_mask:0xf bank_mask:0xf bound_ctrl:1
	s_nop 0
	v_readlane_b32 s0, v5, 0
	v_readlane_b32 s1, v5, 8
	v_readlane_b32 s3, v5, 16
	v_add_f32_e32 v4, s0, v1
	v_rsq_f32_e32 v4, v4
	v_add_f32_e32 v6, s1, v1
	v_rsq_f32_e32 v6, v6
	v_readlane_b32 s4, v5, 24
	v_readlane_b32 s5, v5, 32
	v_readlane_b32 s6, v5, 40
	v_readlane_b32 s7, v5, 48
	v_readlane_b32 s0, v5, 56
	v_pk_mul_f32 v[4:5], v[84:85], v[4:5] op_sel_hi:[1,0]
	s_nop 0
	v_cvt_pk_bf16_f32 v7, v4, v5
	v_pk_mul_f32 v[4:5], v[86:87], v[6:7] op_sel_hi:[1,0]
	v_add_f32_e32 v6, s4, v1
	v_cvt_pk_bf16_f32 v5, v4, v5
	v_add_f32_e32 v4, s3, v1
	v_rsq_f32_e32 v4, v4
	v_rsq_f32_e32 v6, v6
	ds_write2_b32 v114, v7, v5 offset1:68
	s_movk_i32 s3, 0x192
	v_pk_mul_f32 v[4:5], v[94:95], v[4:5] op_sel_hi:[1,0]
	v_cmp_gt_i32_e32 vcc, s3, v167
	v_cvt_pk_bf16_f32 v7, v4, v5
	v_pk_mul_f32 v[4:5], v[100:101], v[6:7] op_sel_hi:[1,0]
	v_add_f32_e32 v6, s6, v1
	v_cvt_pk_bf16_f32 v5, v4, v5
	v_add_f32_e32 v4, s5, v1
	v_rsq_f32_e32 v4, v4
	v_rsq_f32_e32 v6, v6
	ds_write2_b32 v114, v7, v5 offset0:136 offset1:204
	v_pk_mul_f32 v[4:5], v[98:99], v[4:5] op_sel_hi:[1,0]
	s_nop 0
	v_cvt_pk_bf16_f32 v7, v4, v5
	v_pk_mul_f32 v[4:5], v[90:91], v[6:7] op_sel_hi:[1,0]
	v_add_f32_e32 v6, s0, v1
	v_cvt_pk_bf16_f32 v5, v4, v5
	v_add_f32_e32 v4, s7, v1
	v_rsq_f32_e32 v4, v4
	v_rsq_f32_e32 v6, v6
	ds_write2_b32 v8, v7, v5 offset0:16 offset1:84
	s_cselect_b64 s[0:1], -1, 0
	v_pk_mul_f32 v[4:5], v[32:33], v[4:5] op_sel_hi:[1,0]
	v_pk_mul_f32 v[2:3], v[2:3], v[6:7] op_sel_hi:[1,0]
	v_cvt_pk_bf16_f32 v4, v4, v5
	v_cvt_pk_bf16_f32 v2, v2, v3
	s_and_b64 s[4:5], s[0:1], vcc
	ds_write2_b32 v8, v4, v2 offset0:152 offset1:220
	s_and_saveexec_b64 s[0:1], s[4:5]
	s_cbranch_execz .LBB0_312
	s_ashr_i32 s7, s46, 31
	s_lshr_b32 s3, s7, 30
	s_add_i32 s3, s46, s3
	s_ashr_i32 s4, s3, 2
	s_cmpk_gt_i32 s2, 0x2ff
	s_mov_b64 s[2:3], -1
	s_cbranch_scc0 .LBB0_309
	s_lshl_b32 s6, s4, 6
	s_and_b32 s5, s6, 0x7fffff00
	s_mov_b64 s[2:3], 0
